# speedup vs baseline: 1.1205x; 1.0619x over previous
_Z9fc_kernelPKDv8_DF16_S1_Pf:
	s_cmp_gt_u32 s2, 195
	s_cbranch_scc1 .Lfc_exit
	s_load_dwordx4 s[4:7], s[0:1], 0x0
	s_load_dwordx2 s[16:17], s[0:1], 0x10
	v_and_b32_e32 v1, 63, v0
	v_lshrrev_b32_e32 v113, 6, v0
	v_and_b32_e32 v89, 31, v0
	v_bfe_u32 v90, v0, 5, 1
	v_lshlrev_b32_e32 v116, 4, v0
	v_lshlrev_b32_e32 v112, 4, v1
	v_lshlrev_b32_e32 v4, 12, v90
	v_lshl_or_b32 v4, v113, 8, v4
	v_lshl_or_b32 v4, v89, 2, v4
	v_add_u32_e32 v102, 0x1c000, v4
	v_lshlrev_b32_e32 v5, 12, v113
	s_mov_b32 s3, 0x1c000
	v_add3_u32 v103, v5, v112, s3
	v_mul_u32_u24_e32 v6, 0xc3500, v113
	v_add_u32_e32 v104, v6, v112
	v_add_u32_e32 v105, 0x30d40, v104
	v_add_u32_e32 v106, 0x61a80, v104
	v_add_u32_e32 v107, 0x927c0, v104
	v_add_u32_e32 v108, 0x30d400, v104
	v_add_u32_e32 v109, 0x30d400, v105
	v_add_u32_e32 v110, 0x30d400, v106
	v_add_u32_e32 v111, 0x30d400, v107
	v_mul_u32_u24_e32 v7, 0x3800, v113
	v_add_u32_e32 v114, v7, v112
	v_cmp_gt_u32_e64 s[34:35], 20, v1
	s_mul_i32 s3, s2, 0xe000
	v_add_u32_e32 v117, s3, v114
	v_add_u32_e32 v118, 0x1000, v117
	v_add_u32_e32 v119, 0x2000, v117
	v_add_u32_e32 v115, 0x3000, v117
	s_waitcnt lgkmcnt(0)
	global_load_dwordx4 v[32:35], v117, s[4:5]
	global_load_dwordx4 v[36:39], v117, s[4:5] offset:1024
	global_load_dwordx4 v[40:43], v117, s[4:5] offset:2048
	global_load_dwordx4 v[44:47], v117, s[4:5] offset:3072
	global_load_dwordx4 v[48:51], v118, s[4:5]
	global_load_dwordx4 v[52:55], v118, s[4:5] offset:1024
	global_load_dwordx4 v[56:59], v118, s[4:5] offset:2048
	global_load_dwordx4 v[60:63], v118, s[4:5] offset:3072
	global_load_dwordx4 v[64:67], v119, s[4:5]
	global_load_dwordx4 v[68:71], v119, s[4:5] offset:1024
	global_load_dwordx4 v[72:75], v119, s[4:5] offset:2048
	global_load_dwordx4 v[76:79], v119, s[4:5] offset:3072
	global_load_dwordx4 v[80:83], v115, s[4:5]
	global_load_dwordx4 v[84:87], v115, s[4:5] offset:1024
	s_mov_b64 s[30:31], s[6:7]
	global_load_dwordx4 v[152:155], v116, s[30:31]
	s_add_u32 s30, s30, 0x1000
	s_addc_u32 s31, s31, 0
	global_load_dwordx4 v[156:159], v116, s[30:31]
	s_add_u32 s30, s30, 0x1000
	s_addc_u32 s31, s31, 0
	global_load_dwordx4 v[160:163], v116, s[30:31]
	s_add_u32 s30, s30, 0x1000
	s_addc_u32 s31, s31, 0
	global_load_dwordx4 v[164:167], v116, s[30:31]
	s_add_u32 s30, s30, 0x1000
	s_addc_u32 s31, s31, 0
	global_load_dwordx4 v[168:171], v116, s[30:31]
	s_add_u32 s30, s30, 0x1000
	s_addc_u32 s31, s31, 0
	global_load_dwordx4 v[172:175], v116, s[30:31]
	s_add_u32 s30, s30, 0x1000
	s_addc_u32 s31, s31, 0
	global_load_dwordx4 v[176:179], v116, s[30:31]
	s_add_u32 s30, s30, 0x1000
	s_addc_u32 s31, s31, 0
	global_load_dwordx4 v[180:183], v116, s[30:31]
	s_add_u32 s30, s30, 0x1000
	s_addc_u32 s31, s31, 0
	global_load_dwordx4 v[184:187], v116, s[30:31]
	s_add_u32 s30, s30, 0x1000
	s_addc_u32 s31, s31, 0
	global_load_dwordx4 v[188:191], v116, s[30:31]
	s_add_u32 s30, s30, 0x1000
	s_addc_u32 s31, s31, 0
	global_load_dwordx4 v[192:195], v116, s[30:31]
	s_add_u32 s30, s30, 0x1000
	s_addc_u32 s31, s31, 0
	global_load_dwordx4 v[196:199], v116, s[30:31]
	s_add_u32 s30, s30, 0x1000
	s_addc_u32 s31, s31, 0
	global_load_dwordx4 v[200:203], v116, s[30:31]
	s_add_u32 s30, s30, 0x1000
	s_addc_u32 s31, s31, 0
	global_load_dwordx4 v[204:207], v116, s[30:31]
	s_lshl_b32 s3, s2, 10
	s_add_u32 s8, s16, s3
	s_addc_u32 s9, s17, 0
	s_mov_b64 s[24:25], -1
	s_cmp_eq_u32 s2, 195
	s_cselect_b64 s[24:25], s[34:35], s[24:25]
	s_mov_b32 s20, 0
	s_waitcnt vmcnt(0)
	ds_write_b128 v116, v[152:155]
	ds_write_b128 v116, v[156:159] offset:4096
	ds_write_b128 v116, v[160:163] offset:8192
	ds_write_b128 v116, v[164:167] offset:12288
	ds_write_b128 v116, v[168:171] offset:16384
	ds_write_b128 v116, v[172:175] offset:20480
	ds_write_b128 v116, v[176:179] offset:24576
	ds_write_b128 v116, v[180:183] offset:28672
	ds_write_b128 v116, v[184:187] offset:32768
	ds_write_b128 v116, v[188:191] offset:36864
	ds_write_b128 v116, v[192:195] offset:40960
	ds_write_b128 v116, v[196:199] offset:45056
	ds_write_b128 v116, v[200:203] offset:49152
	ds_write_b128 v116, v[204:207] offset:53248
	s_waitcnt lgkmcnt(0)
	s_barrier
.Lfc_seg:
	s_cmp_eq_u32 s20, 15
	s_cbranch_scc1 .Lfc_nopf
	s_add_i32 s3, s20, 1
	s_mul_i32 s3, s3, 0xe000
	s_add_u32 s30, s6, s3
	s_addc_u32 s31, s7, 0
	global_load_dwordx4 v[152:155], v116, s[30:31]
	s_add_u32 s30, s30, 0x1000
	s_addc_u32 s31, s31, 0
	global_load_dwordx4 v[156:159], v116, s[30:31]
	s_add_u32 s30, s30, 0x1000
	s_addc_u32 s31, s31, 0
	global_load_dwordx4 v[160:163], v116, s[30:31]
	s_add_u32 s30, s30, 0x1000
	s_addc_u32 s31, s31, 0
	global_load_dwordx4 v[164:167], v116, s[30:31]
	s_add_u32 s30, s30, 0x1000
	s_addc_u32 s31, s31, 0
	global_load_dwordx4 v[168:171], v116, s[30:31]
	s_add_u32 s30, s30, 0x1000
	s_addc_u32 s31, s31, 0
	global_load_dwordx4 v[172:175], v116, s[30:31]
	s_add_u32 s30, s30, 0x1000
	s_addc_u32 s31, s31, 0
	global_load_dwordx4 v[176:179], v116, s[30:31]
	s_add_u32 s30, s30, 0x1000
	s_addc_u32 s31, s31, 0
	global_load_dwordx4 v[180:183], v116, s[30:31]
	s_add_u32 s30, s30, 0x1000
	s_addc_u32 s31, s31, 0
	global_load_dwordx4 v[184:187], v116, s[30:31]
	s_add_u32 s30, s30, 0x1000
	s_addc_u32 s31, s31, 0
	global_load_dwordx4 v[188:191], v116, s[30:31]
	s_add_u32 s30, s30, 0x1000
	s_addc_u32 s31, s31, 0
	global_load_dwordx4 v[192:195], v116, s[30:31]
	s_add_u32 s30, s30, 0x1000
	s_addc_u32 s31, s31, 0
	global_load_dwordx4 v[196:199], v116, s[30:31]
	s_add_u32 s30, s30, 0x1000
	s_addc_u32 s31, s31, 0
	global_load_dwordx4 v[200:203], v116, s[30:31]
	s_add_u32 s30, s30, 0x1000
	s_addc_u32 s31, s31, 0
	global_load_dwordx4 v[204:207], v116, s[30:31]
.Lfc_nopf:
	s_and_b32 s3, s20, 1
	s_mul_i32 s3, s3, 0xe000
	v_add_u32_e32 v88, s3, v112
	s_mov_b32 s0, 0
.Lfc_step:
	ds_read_b128 v[120:123], v88
	ds_read_b128 v[124:127], v88 offset:1024
	ds_read_b128 v[128:131], v88 offset:2048
	ds_read_b128 v[132:135], v88 offset:3072
	ds_read_b128 v[136:139], v88 offset:4096
	ds_read_b128 v[140:143], v88 offset:5120
	ds_read_b128 v[144:147], v88 offset:6144
	v_add_u32_e32 v88, 0x1c00, v88
	s_waitcnt lgkmcnt(6)
	v_mfma_f32_32x32x16_f16 v[0:15], v[120:123], v[32:35], 0
	v_mfma_f32_32x32x16_f16 v[16:31], v[120:123], v[60:63], 0
	s_waitcnt lgkmcnt(5)
	v_mfma_f32_32x32x16_f16 v[0:15], v[124:127], v[36:39], v[0:15]
	v_mfma_f32_32x32x16_f16 v[16:31], v[124:127], v[64:67], v[16:31]
	s_waitcnt lgkmcnt(4)
	v_mfma_f32_32x32x16_f16 v[0:15], v[128:131], v[40:43], v[0:15]
	v_mfma_f32_32x32x16_f16 v[16:31], v[128:131], v[68:71], v[16:31]
	s_waitcnt lgkmcnt(3)
	v_mfma_f32_32x32x16_f16 v[0:15], v[132:135], v[44:47], v[0:15]
	v_mfma_f32_32x32x16_f16 v[16:31], v[132:135], v[72:75], v[16:31]
	s_waitcnt lgkmcnt(2)
	v_mfma_f32_32x32x16_f16 v[0:15], v[136:139], v[48:51], v[0:15]
	v_mfma_f32_32x32x16_f16 v[16:31], v[136:139], v[76:79], v[16:31]
	s_waitcnt lgkmcnt(1)
	v_mfma_f32_32x32x16_f16 v[0:15], v[140:143], v[52:55], v[0:15]
	v_mfma_f32_32x32x16_f16 v[16:31], v[140:143], v[80:83], v[16:31]
	s_waitcnt lgkmcnt(0)
	v_mfma_f32_32x32x16_f16 v[0:15], v[144:147], v[56:59], v[0:15]
	v_mfma_f32_32x32x16_f16 v[16:31], v[144:147], v[84:87], v[16:31]
	s_nop 11
	s_barrier
	ds_write_b32 v102, v0 offset:0
	ds_write_b32 v102, v1 offset:1024
	ds_write_b32 v102, v2 offset:2048
	ds_write_b32 v102, v3 offset:3072
	ds_write_b32 v102, v4 offset:8192
	ds_write_b32 v102, v5 offset:9216
	ds_write_b32 v102, v6 offset:10240
	ds_write_b32 v102, v7 offset:11264
	ds_write_b32 v102, v16 offset:128
	ds_write_b32 v102, v17 offset:1152
	ds_write_b32 v102, v18 offset:2176
	ds_write_b32 v102, v19 offset:3200
	ds_write_b32 v102, v20 offset:8320
	ds_write_b32 v102, v21 offset:9344
	ds_write_b32 v102, v22 offset:10368
	ds_write_b32 v102, v23 offset:11392
	s_waitcnt lgkmcnt(0)
	s_barrier
	ds_read_b128 v[0:3], v103
	ds_read_b128 v[4:7], v103 offset:1024
	ds_read_b128 v[16:19], v103 offset:2048
	ds_read_b128 v[20:23], v103 offset:3072
	s_mov_b64 exec, s[24:25]
	s_waitcnt lgkmcnt(3)
	global_store_dwordx4 v104, v[0:3], s[8:9]
	s_waitcnt lgkmcnt(2)
	global_store_dwordx4 v105, v[4:7], s[8:9]
	s_waitcnt lgkmcnt(1)
	global_store_dwordx4 v106, v[16:19], s[8:9]
	s_waitcnt lgkmcnt(0)
	global_store_dwordx4 v107, v[20:23], s[8:9]
	s_mov_b64 exec, -1
	s_barrier
	ds_write_b32 v102, v8 offset:0
	ds_write_b32 v102, v9 offset:1024
	ds_write_b32 v102, v10 offset:2048
	ds_write_b32 v102, v11 offset:3072
	ds_write_b32 v102, v12 offset:8192
	ds_write_b32 v102, v13 offset:9216
	ds_write_b32 v102, v14 offset:10240
	ds_write_b32 v102, v15 offset:11264
	ds_write_b32 v102, v24 offset:128
	ds_write_b32 v102, v25 offset:1152
	ds_write_b32 v102, v26 offset:2176
	ds_write_b32 v102, v27 offset:3200
	ds_write_b32 v102, v28 offset:8320
	ds_write_b32 v102, v29 offset:9344
	ds_write_b32 v102, v30 offset:10368
	ds_write_b32 v102, v31 offset:11392
	s_waitcnt lgkmcnt(0)
	s_barrier
	ds_read_b128 v[8:11], v103
	ds_read_b128 v[12:15], v103 offset:1024
	ds_read_b128 v[24:27], v103 offset:2048
	ds_read_b128 v[28:31], v103 offset:3072
	s_mov_b64 exec, s[24:25]
	s_waitcnt lgkmcnt(3)
	global_store_dwordx4 v108, v[8:11], s[8:9]
	s_waitcnt lgkmcnt(2)
	global_store_dwordx4 v109, v[12:15], s[8:9]
	s_waitcnt lgkmcnt(1)
	global_store_dwordx4 v110, v[24:27], s[8:9]
	s_waitcnt lgkmcnt(0)
	global_store_dwordx4 v111, v[28:31], s[8:9]
	s_mov_b64 exec, -1
	s_add_u32 s8, s8, 0x61a800
	s_addc_u32 s9, s9, 0
	s_add_i32 s0, s0, 1
	s_cmp_lt_u32 s0, 8
	s_cbranch_scc1 .Lfc_step
	s_cmp_eq_u32 s20, 15
	s_cbranch_scc1 .Lfc_exit
	s_waitcnt vmcnt(63)
	s_add_i32 s3, s20, 1
	s_and_b32 s3, s3, 1
	s_mul_i32 s3, s3, 0xe000
	v_add_u32_e32 v117, s3, v116
	ds_write_b128 v117, v[152:155]
	ds_write_b128 v117, v[156:159] offset:4096
	ds_write_b128 v117, v[160:163] offset:8192
	ds_write_b128 v117, v[164:167] offset:12288
	ds_write_b128 v117, v[168:171] offset:16384
	ds_write_b128 v117, v[172:175] offset:20480
	ds_write_b128 v117, v[176:179] offset:24576
	ds_write_b128 v117, v[180:183] offset:28672
	ds_write_b128 v117, v[184:187] offset:32768
	ds_write_b128 v117, v[188:191] offset:36864
	ds_write_b128 v117, v[192:195] offset:40960
	ds_write_b128 v117, v[196:199] offset:45056
	ds_write_b128 v117, v[200:203] offset:49152
	ds_write_b128 v117, v[204:207] offset:53248
	s_waitcnt lgkmcnt(0)
	s_barrier
	s_add_i32 s20, s20, 1
	s_branch .Lfc_seg

	.amdhsa_kernel _Z9fc_kernelPKDv8_DF16_S1_Pf
		.amdhsa_group_segment_fixed_size 131072
		.amdhsa_private_segment_fixed_size 0
		.amdhsa_kernarg_size 24
		.amdhsa_user_sgpr_count 2
		.amdhsa_user_sgpr_dispatch_ptr 0
		.amdhsa_user_sgpr_queue_ptr 0
		.amdhsa_user_sgpr_kernarg_segment_ptr 1
		.amdhsa_user_sgpr_dispatch_id 0
		.amdhsa_user_sgpr_kernarg_preload_length 0
		.amdhsa_user_sgpr_kernarg_preload_offset 0
		.amdhsa_user_sgpr_private_segment_size 0
		.amdhsa_uses_dynamic_stack 0
		.amdhsa_enable_private_segment 0
		.amdhsa_system_sgpr_workgroup_id_x 1
		.amdhsa_system_sgpr_workgroup_id_y 0
		.amdhsa_system_sgpr_workgroup_id_z 0
		.amdhsa_system_sgpr_workgroup_info 0
		.amdhsa_system_vgpr_workitem_id 0
		.amdhsa_next_free_vgpr 208
		.amdhsa_next_free_sgpr 96
		.amdhsa_accum_offset 208
		.amdhsa_reserve_vcc 1
		.amdhsa_float_round_mode_32 0
		.amdhsa_float_round_mode_16_64 0
		.amdhsa_float_denorm_mode_32 3
		.amdhsa_float_denorm_mode_16_64 3
		.amdhsa_dx10_clamp 1
		.amdhsa_ieee_mode 1
		.amdhsa_fp16_overflow 0
		.amdhsa_tg_split 0
		.amdhsa_exception_fp_ieee_invalid_op 0
		.amdhsa_exception_fp_denorm_src 0
		.amdhsa_exception_fp_ieee_div_zero 0
		.amdhsa_exception_fp_ieee_overflow 0
		.amdhsa_exception_fp_ieee_underflow 0
		.amdhsa_exception_fp_ieee_inexact 0
		.amdhsa_exception_int_div_zero 0
	.end_amdhsa_kernel

amdhsa.kernels:
  - .agpr_count:     0
    .args:
      - .actual_access:  read_only
        .address_space:  global
        .offset:         0
        .size:           8
        .value_kind:     global_buffer
      - .actual_access:  read_only
        .address_space:  global
        .offset:         8
        .size:           8
        .value_kind:     global_buffer
      - .actual_access:  read_only
        .address_space:  global
        .offset:         16
        .size:           8
        .value_kind:     global_buffer
      - .actual_access:  read_only
        .address_space:  global
        .offset:         24
        .size:           8
        .value_kind:     global_buffer
      - .actual_access:  read_only
        .address_space:  global
        .offset:         32
        .size:           8
        .value_kind:     global_buffer
      - .actual_access:  write_only
        .address_space:  global
        .offset:         40
        .size:           8
        .value_kind:     global_buffer
      - .actual_access:  write_only
        .address_space:  global
        .offset:         48
        .size:           8
        .value_kind:     global_buffer
      - .actual_access:  write_only
        .address_space:  global
        .offset:         56
        .size:           8
        .value_kind:     global_buffer
    .group_segment_fixed_size: 0
    .kernarg_segment_align: 8
    .kernarg_segment_size: 64
    .language:       OpenCL C
    .language_version:
      - 2
      - 0
    .max_flat_workgroup_size: 256
    .name:           _Z11prep_kernelPKfS0_S0_S0_S0_PDv8_DF16_S2_Pi
    .private_segment_fixed_size: 0
    .sgpr_count:     26
    .sgpr_spill_count: 0
    .symbol:         _Z11prep_kernelPKfS0_S0_S0_S0_PDv8_DF16_S2_Pi.kd
    .uniform_work_group_size: 1
    .uses_dynamic_stack: false
    .vgpr_count:     18
    .vgpr_spill_count: 0
    .wavefront_size: 64
  - .agpr_count:     0
    .args:
      - .actual_access:  read_only
        .address_space:  global
        .offset:         0
        .size:           8
        .value_kind:     global_buffer
      - .actual_access:  read_only
        .address_space:  global
        .offset:         8
        .size:           8
        .value_kind:     global_buffer
      - .actual_access:  read_only
        .address_space:  global
        .offset:         16
        .size:           8
        .value_kind:     global_buffer
      - .actual_access:  read_only
        .address_space:  global
        .offset:         24
        .size:           8
        .value_kind:     global_buffer
      - .actual_access:  read_only
        .address_space:  global
        .offset:         32
        .size:           8
        .value_kind:     global_buffer
      - .actual_access:  read_only
        .address_space:  global
        .offset:         40
        .size:           8
        .value_kind:     global_buffer
      - .actual_access:  read_only
        .address_space:  global
        .offset:         48
        .size:           8
        .value_kind:     global_buffer
      - .actual_access:  read_only
        .address_space:  global
        .offset:         56
        .size:           8
        .value_kind:     global_buffer
      - .actual_access:  read_only
        .address_space:  global
        .offset:         64
        .size:           8
        .value_kind:     global_buffer
      - .actual_access:  read_only
        .address_space:  global
        .offset:         72
        .size:           8
        .value_kind:     global_buffer
      - .actual_access:  read_only
        .address_space:  global
        .offset:         80
        .size:           8
        .value_kind:     global_buffer
      - .actual_access:  read_only
        .address_space:  global
        .offset:         88
        .size:           8
        .value_kind:     global_buffer
      - .actual_access:  read_only
        .address_space:  global
        .offset:         96
        .size:           8
        .value_kind:     global_buffer
      - .actual_access:  read_only
        .address_space:  global
        .offset:         104
        .size:           8
        .value_kind:     global_buffer
      - .actual_access:  write_only
        .address_space:  global
        .offset:         112
        .size:           8
        .value_kind:     global_buffer
      - .offset:         120
        .size:           4
        .value_kind:     by_value
      - .actual_access:  read_only
        .address_space:  global
        .offset:         128
        .size:           8
        .value_kind:     global_buffer
      - .actual_access:  read_only
        .address_space:  global
        .offset:         136
        .size:           8
        .value_kind:     global_buffer
      - .actual_access:  write_only
        .address_space:  global
        .offset:         144
        .size:           8
        .value_kind:     global_buffer
      - .actual_access:  read_only
        .address_space:  global
        .offset:         152
        .size:           8
        .value_kind:     global_buffer
      - .actual_access:  read_only
        .address_space:  global
        .offset:         160
        .size:           8
        .value_kind:     global_buffer
      - .address_space:  global
        .offset:         168
        .size:           8
        .value_kind:     global_buffer
      - .actual_access:  write_only
        .address_space:  global
        .offset:         176
        .size:           8
        .value_kind:     global_buffer
      - .address_space:  global
        .offset:         184
        .size:           8
        .value_kind:     global_buffer
      - .actual_access:  write_only
        .address_space:  global
        .offset:         192
        .size:           8
        .value_kind:     global_buffer
      - .actual_access:  write_only
        .address_space:  global
        .offset:         200
        .size:           8
        .value_kind:     global_buffer
    .group_segment_fixed_size: 21760
    .kernarg_segment_align: 8
    .kernarg_segment_size: 208
    .language:       OpenCL C
    .language_version:
      - 2
      - 0
    .max_flat_workgroup_size: 256
    .name:           _Z12embed_kernelPKiS0_S0_S0_S0_PKfS2_S2_S2_S2_S2_S2_S2_PKDv8_DF16_PfiS2_S2_PS3_S0_S0_PiS8_S8_P15HIP_vector_typeIiLj2EES8_
    .private_segment_fixed_size: 0
    .sgpr_count:     44
    .sgpr_spill_count: 0
    .symbol:         _Z12embed_kernelPKiS0_S0_S0_S0_PKfS2_S2_S2_S2_S2_S2_S2_PKDv8_DF16_PfiS2_S2_PS3_S0_S0_PiS8_S8_P15HIP_vector_typeIiLj2EES8_.kd
    .uniform_work_group_size: 1
    .uses_dynamic_stack: false
    .vgpr_count:     166
    .vgpr_spill_count: 0
    .wavefront_size: 64
  - .agpr_count:     0
    .args:
      - .actual_access:  read_only
        .address_space:  global
        .offset:         0
        .size:           8
        .value_kind:     global_buffer
      - .actual_access:  read_only
        .address_space:  global
        .offset:         8
        .size:           8
        .value_kind:     global_buffer
      - .actual_access:  read_only
        .address_space:  global
        .offset:         16
        .size:           8
        .value_kind:     global_buffer
      - .actual_access:  read_only
        .address_space:  global
        .offset:         24
        .size:           8
        .value_kind:     global_buffer
      - .actual_access:  read_only
        .address_space:  global
        .offset:         32
        .size:           8
        .value_kind:     global_buffer
      - .actual_access:  read_only
        .address_space:  global
        .offset:         40
        .size:           8
        .value_kind:     global_buffer
      - .actual_access:  read_only
        .address_space:  global
        .offset:         48
        .size:           8
        .value_kind:     global_buffer
      - .actual_access:  read_only
        .address_space:  global
        .offset:         56
        .size:           8
        .value_kind:     global_buffer
      - .actual_access:  write_only
        .address_space:  global
        .offset:         64
        .size:           8
        .value_kind:     global_buffer
      - .offset:         72
        .size:           4
        .value_kind:     by_value
    .group_segment_fixed_size: 30720
    .kernarg_segment_align: 8
    .kernarg_segment_size: 76
    .language:       OpenCL C
    .language_version:
      - 2
      - 0
    .max_flat_workgroup_size: 256
    .name:           _Z10gru_kernelPKfPKiS2_S2_PK15HIP_vector_typeIiLj2EEPKDv8_DF16_S0_S0_Pfi
    .private_segment_fixed_size: 0
    .sgpr_count:     31
    .sgpr_spill_count: 0
    .symbol:         _Z10gru_kernelPKfPKiS2_S2_PK15HIP_vector_typeIiLj2EEPKDv8_DF16_S0_S0_Pfi.kd
    .uniform_work_group_size: 1
    .uses_dynamic_stack: false
    .vgpr_count:     231
    .vgpr_spill_count: 0
    .wavefront_size: 64
  - .agpr_count:     0
    .args:
      - .actual_access:  read_only
        .address_space:  global
        .offset:         0
        .size:           8
        .value_kind:     global_buffer
      - .actual_access:  read_only
        .address_space:  global
        .offset:         8
        .size:           8
        .value_kind:     global_buffer
      - .actual_access:  write_only
        .address_space:  global
        .offset:         16
        .size:           8
        .value_kind:     global_buffer
    .group_segment_fixed_size: 1024
    .kernarg_segment_align: 8
    .kernarg_segment_size: 24
    .language:       OpenCL C
    .language_version:
      - 2
      - 0
    .max_flat_workgroup_size: 256
    .name:           _Z11pool_kernelPKfPKiPDF16_
    .private_segment_fixed_size: 0
    .sgpr_count:     26
    .sgpr_spill_count: 0
    .symbol:         _Z11pool_kernelPKfPKiPDF16_.kd
    .uniform_work_group_size: 1
    .uses_dynamic_stack: false
    .vgpr_count:     31
    .vgpr_spill_count: 0
    .wavefront_size: 64
  - .agpr_count:     0
    .args:
      - .actual_access:  read_only
        .address_space:  global
        .offset:         0
        .size:           8
        .value_kind:     global_buffer
      - .actual_access:  read_only
        .address_space:  global
        .offset:         8
        .size:           8
        .value_kind:     global_buffer
      - .actual_access:  write_only
        .address_space:  global
        .offset:         16
        .size:           8
        .value_kind:     global_buffer
    .group_segment_fixed_size: 131072
    .kernarg_segment_align: 8
    .kernarg_segment_size: 24
    .language:       OpenCL C
    .language_version:
      - 2
      - 0
    .max_flat_workgroup_size: 256
    .name:           _Z9fc_kernelPKDv8_DF16_S1_Pf
    .private_segment_fixed_size: 0
    .sgpr_count:     17
    .sgpr_spill_count: 0
    .symbol:         _Z9fc_kernelPKDv8_DF16_S1_Pf.kd
    .uniform_work_group_size: 1
    .uses_dynamic_stack: false
    .vgpr_count:     208
    .vgpr_spill_count: 0
    .wavefront_size: 64
